# speedup vs baseline: 1.0239x; 1.0069x over previous
_Z5k_decPKiPKDF16_S2_PKfS4_S4_Pf:
	s_load_dword s3, s[0:1], 0x44
	s_load_dword s6, s[0:1], 0x38
	s_load_dwordx2 s[4:5], s[0:1], 0x0
	s_load_dwordx8 s[28:35], s[0:1], 0x8
	s_load_dwordx4 s[12:15], s[0:1], 0x28
	v_and_b32_e32 v1, 15, v0
	v_and_b32_e32 v64, 63, v0
	v_lshlrev_b32_e32 v96, 3, v1
	v_lshrrev_b32_e32 v4, 3, v0
	v_and_b32_e32 v4, 4, v4
	v_or_b32_e32 v96, v96, v4
	v_mov_b32_e32 v97, 0
	v_and_b32_e32 v104, 16, v0
	v_lshlrev_b32_e32 v6, 7, v0
	v_lshlrev_b32_e32 v7, 2, v64
	s_movk_i32 s16, 0x6000
	v_and_or_b32 v103, v6, s16, v7
	v_mov_b32_e32 v219, 0
	s_movk_i32 s19, 0x3d08
	s_waitcnt lgkmcnt(0)
	s_and_b32 s3, s3, 0xffff
	s_mul_i32 s2, s2, s3
	v_add_u32_e32 v5, s2, v0
	s_mul_i32 s6, s6, s3
	v_lshrrev_b32_e32 v102, 6, v5
	s_lshr_b32 s18, s6, 6
	v_readfirstlane_b32 s23, v102
	v_lshl_add_u64 v[2:3], s[4:5], 0, v[96:97]
	s_mov_b32 s16, 0xf4240
	v_cmp_gt_u32_e32 vcc, s16, v5
	s_and_saveexec_b64 s[22:23], vcc
	s_cbranch_execz .LBB2_3
	v_mov_b32_e32 v222, v2
	v_mov_b32_e32 v223, v3
	v_min_u32_e32 v218, s19, v102
	v_lshlrev_b32_e32 v218, 9, v218
	v_lshl_add_u64 v[216:217], v[222:223], 0, v[218:219]
	global_load_dword v65, v[216:217], off nt
	global_load_dword v80, v[216:217], off offset:128 nt
	global_load_dword v81, v[216:217], off offset:256 nt
	global_load_dword v82, v[216:217], off offset:384 nt
	v_add_u32_e32 v220, s18, v102
	v_min_u32_e32 v218, s19, v220
	v_lshlrev_b32_e32 v218, 9, v218
	v_lshl_add_u64 v[216:217], v[222:223], 0, v[218:219]
	global_load_dword v100, v[216:217], off nt
	global_load_dword v101, v[216:217], off offset:128 nt
	global_load_dword v98, v[216:217], off offset:256 nt
	global_load_dword v99, v[216:217], off offset:384 nt
	s_mov_b32 s8, s28
	s_and_b32 s9, s29, 0xffff
	s_mov_b32 s10, 0x30d400
	s_mov_b32 s11, 0x20000
	s_mov_b64 s[36:37], 0x1000
	v_and_b32_e32 v96, 48, v64
	v_lshlrev_b32_e32 v221, 6, v1
	v_lshlrev_b32_e32 v211, 2, v1
	v_lshlrev_b32_e32 v214, 4, v0
	v_add_u32_e32 v215, 0x1000, v214
	v_lshl_add_u32 v134, v1, 6, v96
	v_add_u32_e32 v134, 0x9000, v134
	v_add_u32_e32 v133, 0x9000, v214
	v_lshl_or_b32 v221, v102, 6, v64
	v_lshrrev_b32_e32 v213, 4, v64
	v_cmp_gt_u32_e32 vcc, 16, v64
	v_and_b32_e32 v210, 31, v64
	v_lshlrev_b32_e32 v210, 4, v210
	s_mov_b32 s38, -1
	s_mov_b32 s39, 0
	s_mov_b64 exec, s[38:39]
	global_load_dwordx4 v[126:129], v210, s[32:33]
	s_mov_b32 s38, 0
	s_mov_b32 s39, -1
	s_mov_b64 exec, s[38:39]
	global_load_dwordx4 v[126:129], v210, s[34:35]
	s_mov_b64 exec, -1
	global_load_dwordx4 v[32:35], v214, s[30:31]
	global_load_dwordx4 v[36:39], v215, s[30:31]
	s_load_dword s12, s[12:13], 0x0
	s_waitcnt vmcnt(8)
	v_lshl_or_b32 v216, v65, 5, v104
	v_lshl_or_b32 v217, v80, 5, v104
	v_lshl_or_b32 v218, v81, 5, v104
	v_lshl_or_b32 v212, v82, 5, v104
	buffer_load_dwordx4 v[92:95], v216, s[8:11], 0 offen
	buffer_load_dwordx4 v[88:91], v217, s[8:11], 0 offen
	buffer_load_dwordx4 v[84:87], v218, s[8:11], 0 offen
	buffer_load_dwordx4 v[80:83], v212, s[8:11], 0 offen
	s_lshl_b32 s21, s18, 6
	s_mov_b32 s20, 2
	s_mov_b64 s[16:17], 0
	v_cmp_eq_u32_e64 s[0:1], 1, v213
	v_cmp_eq_u32_e64 s[2:3], 2, v213
	v_cmp_eq_u32_e64 s[4:5], 3, v213
	v_mov_b32_e32 v96, v221
	v_mov_b32_e32 v97, 0
	s_waitcnt vmcnt(4)
	v_lshrrev_b32_e32 v210, 6, v0
	v_lshlrev_b32_e32 v210, 10, v210
	v_add_u32_e32 v210, 0x8000, v210
	v_lshl_add_u32 v130, v64, 4, v210
	v_lshl_add_u32 v131, v213, 4, v210
	v_add_u32_e32 v132, v211, v210
	ds_write_b128 v130, v[126:129]
	ds_write_b128 v133, v[32:35]
	ds_write_b128 v133, v[36:39] offset:4096
	ds_read_b128 v[68:71], v131 offset:512
	ds_read_b128 v[72:75], v131 offset:576
	ds_read_b128 v[76:79], v131 offset:640
	ds_read_b128 v[106:109], v131 offset:704
	ds_read_b128 v[110:113], v131 offset:768
	ds_read_b128 v[114:117], v131 offset:832
	ds_read_b128 v[118:121], v131 offset:896
	ds_read_b128 v[122:125], v131 offset:960
	s_waitcnt lgkmcnt(0)
	s_barrier
	ds_read_b32 v148, v132 offset:512
	ds_read_b32 v149, v132 offset:576
	ds_read_b32 v150, v132 offset:640
	ds_read_b32 v151, v132 offset:704
	ds_read_b32 v152, v132 offset:768
	ds_read_b32 v153, v132 offset:832
	ds_read_b32 v154, v132 offset:896
	ds_read_b32 v155, v132 offset:960
	ds_read_b32 v156, v132 offset:0
	ds_read_b32 v157, v132 offset:64
	ds_read_b32 v158, v132 offset:128
	ds_read_b32 v159, v132 offset:192
	s_waitcnt lgkmcnt(0)
	ds_read_b32 v160, v132 offset:256
	ds_read_b32 v161, v132 offset:320
	ds_read_b32 v162, v132 offset:384
	ds_read_b32 v163, v132 offset:448
	ds_read_b128 v[0:3], v131 offset:0
	ds_read_b128 v[4:7], v131 offset:64
	ds_read_b128 v[8:11], v131 offset:128
	ds_read_b128 v[12:15], v131 offset:192
	ds_read_b128 v[16:19], v131 offset:256
	ds_read_b128 v[20:23], v131 offset:320
	ds_read_b128 v[24:27], v131 offset:384
	ds_read_b128 v[28:31], v131 offset:448
	s_waitcnt lgkmcnt(0)
	ds_read_b128 v[32:35], v134
	ds_read_b128 v[36:39], v134 offset:1024
	ds_read_b128 v[40:43], v134 offset:2048
	ds_read_b128 v[44:47], v134 offset:3072
	ds_read_b128 v[48:51], v134 offset:4096
	ds_read_b128 v[52:55], v134 offset:5120
	ds_read_b128 v[56:59], v134 offset:6144
	ds_read_b128 v[60:63], v134 offset:7168
	v_cvt_pk_f16_f32 v67, v74, v75
	v_cvt_pk_f16_f32 v66, v72, v73
	v_cvt_pk_f16_f32 v65, v70, v71
	v_cvt_pk_f16_f32 v64, v68, v69
	v_cvt_pk_f16_f32 v71, v108, v109
	v_cvt_pk_f16_f32 v70, v106, v107
	v_cvt_pk_f16_f32 v69, v78, v79
	v_cvt_pk_f16_f32 v68, v76, v77
	v_cvt_pk_f16_f32 v75, v116, v117
	v_cvt_pk_f16_f32 v74, v114, v115
	v_cvt_pk_f16_f32 v73, v112, v113
	v_cvt_pk_f16_f32 v72, v110, v111
	v_cvt_pk_f16_f32 v79, v124, v125
	v_cvt_pk_f16_f32 v78, v122, v123
	v_cvt_pk_f16_f32 v77, v120, v121
	v_cvt_pk_f16_f32 v76, v118, v119
	v_mov_b32_e32 v167, 0x38003800
	v_pk_mul_f16 v64, v64, v167
	v_pk_mul_f16 v65, v65, v167
	v_pk_mul_f16 v66, v66, v167
	v_pk_mul_f16 v67, v67, v167
	v_pk_mul_f16 v68, v68, v167
	v_pk_mul_f16 v69, v69, v167
	v_pk_mul_f16 v70, v70, v167
	v_pk_mul_f16 v71, v71, v167
	v_pk_mul_f16 v72, v72, v167
	v_pk_mul_f16 v73, v73, v167
	v_pk_mul_f16 v74, v74, v167
	v_pk_mul_f16 v75, v75, v167
	v_pk_mul_f16 v76, v76, v167
	v_pk_mul_f16 v77, v77, v167
	v_pk_mul_f16 v78, v78, v167
	v_pk_mul_f16 v79, v79, v167
	v_cvt_f16_f32_e32 v148, v148
	v_cvt_f16_f32_e32 v149, v149
	v_cvt_f16_f32_e32 v150, v150
	v_cvt_f16_f32_e32 v151, v151
	v_cvt_f16_f32_e32 v152, v152
	v_cvt_f16_f32_e32 v153, v153
	v_cvt_f16_f32_e32 v154, v154
	v_cvt_f16_f32_e32 v155, v155
	v_cvt_f32_f16_e32 v148, v148
	v_cvt_f32_f16_e32 v149, v149
	v_cvt_f32_f16_e32 v150, v150
	v_cvt_f32_f16_e32 v151, v151
	v_cvt_f32_f16_e32 v152, v152
	v_cvt_f32_f16_e32 v153, v153
	v_cvt_f32_f16_e32 v154, v154
	v_cvt_f32_f16_e32 v155, v155
	v_mul_f32_e32 v148, 0.5, v148
	v_mul_f32_e32 v149, 0.5, v149
	v_mul_f32_e32 v150, 0.5, v150
	v_mul_f32_e32 v151, 0.5, v151
	v_mul_f32_e32 v152, 0.5, v152
	v_mul_f32_e32 v153, 0.5, v153
	v_mul_f32_e32 v154, 0.5, v154
	v_mul_f32_e32 v155, 0.5, v155
	v_mov_b32_e32 v140, 0
	v_mov_b32_e32 v141, 0
	v_mov_b32_e32 v142, 0
	v_mov_b32_e32 v143, 0
	v_mov_b32_e32 v144, 0
	v_mov_b32_e32 v145, 0
	v_mov_b32_e32 v146, 0
	v_mov_b32_e32 v147, 0
	v_mov_b32_e32 v166, 0
	s_waitcnt lgkmcnt(0)
	v_cvt_f32_f16_e32 v164, v32
	v_cvt_f32_f16_sdwa v165, v32 dst_sel:DWORD dst_unused:UNUSED_PAD src0_sel:WORD_1
	v_fmac_f32_e32 v140, v148, v164
	v_fmac_f32_e32 v141, v148, v165
	v_cvt_f32_f16_e32 v164, v33
	v_cvt_f32_f16_sdwa v165, v33 dst_sel:DWORD dst_unused:UNUSED_PAD src0_sel:WORD_1
	v_fmac_f32_e32 v142, v148, v164
	v_fmac_f32_e32 v143, v148, v165
	v_cvt_f32_f16_e32 v164, v34
	v_cvt_f32_f16_sdwa v165, v34 dst_sel:DWORD dst_unused:UNUSED_PAD src0_sel:WORD_1
	v_fmac_f32_e32 v144, v148, v164
	v_fmac_f32_e32 v145, v148, v165
	v_cvt_f32_f16_e32 v164, v35
	v_cvt_f32_f16_sdwa v165, v35 dst_sel:DWORD dst_unused:UNUSED_PAD src0_sel:WORD_1
	v_fmac_f32_e32 v146, v148, v164
	v_fmac_f32_e32 v147, v148, v165
	v_fmac_f32_e32 v166, v148, v156
	v_cvt_f32_f16_e32 v164, v36
	v_cvt_f32_f16_sdwa v165, v36 dst_sel:DWORD dst_unused:UNUSED_PAD src0_sel:WORD_1
	v_fmac_f32_e32 v140, v149, v164
	v_fmac_f32_e32 v141, v149, v165
	v_cvt_f32_f16_e32 v164, v37
	v_cvt_f32_f16_sdwa v165, v37 dst_sel:DWORD dst_unused:UNUSED_PAD src0_sel:WORD_1
	v_fmac_f32_e32 v142, v149, v164
	v_fmac_f32_e32 v143, v149, v165
	v_cvt_f32_f16_e32 v164, v38
	v_cvt_f32_f16_sdwa v165, v38 dst_sel:DWORD dst_unused:UNUSED_PAD src0_sel:WORD_1
	v_fmac_f32_e32 v144, v149, v164
	v_fmac_f32_e32 v145, v149, v165
	v_cvt_f32_f16_e32 v164, v39
	v_cvt_f32_f16_sdwa v165, v39 dst_sel:DWORD dst_unused:UNUSED_PAD src0_sel:WORD_1
	v_fmac_f32_e32 v146, v149, v164
	v_fmac_f32_e32 v147, v149, v165
	v_fmac_f32_e32 v166, v149, v157
	v_cvt_f32_f16_e32 v164, v40
	v_cvt_f32_f16_sdwa v165, v40 dst_sel:DWORD dst_unused:UNUSED_PAD src0_sel:WORD_1
	v_fmac_f32_e32 v140, v150, v164
	v_fmac_f32_e32 v141, v150, v165
	v_cvt_f32_f16_e32 v164, v41
	v_cvt_f32_f16_sdwa v165, v41 dst_sel:DWORD dst_unused:UNUSED_PAD src0_sel:WORD_1
	v_fmac_f32_e32 v142, v150, v164
	v_fmac_f32_e32 v143, v150, v165
	v_cvt_f32_f16_e32 v164, v42
	v_cvt_f32_f16_sdwa v165, v42 dst_sel:DWORD dst_unused:UNUSED_PAD src0_sel:WORD_1
	v_fmac_f32_e32 v144, v150, v164
	v_fmac_f32_e32 v145, v150, v165
	v_cvt_f32_f16_e32 v164, v43
	v_cvt_f32_f16_sdwa v165, v43 dst_sel:DWORD dst_unused:UNUSED_PAD src0_sel:WORD_1
	v_fmac_f32_e32 v146, v150, v164
	v_fmac_f32_e32 v147, v150, v165
	v_fmac_f32_e32 v166, v150, v158
	v_cvt_f32_f16_e32 v164, v44
	v_cvt_f32_f16_sdwa v165, v44 dst_sel:DWORD dst_unused:UNUSED_PAD src0_sel:WORD_1
	v_fmac_f32_e32 v140, v151, v164
	v_fmac_f32_e32 v141, v151, v165
	v_cvt_f32_f16_e32 v164, v45
	v_cvt_f32_f16_sdwa v165, v45 dst_sel:DWORD dst_unused:UNUSED_PAD src0_sel:WORD_1
	v_fmac_f32_e32 v142, v151, v164
	v_fmac_f32_e32 v143, v151, v165
	v_cvt_f32_f16_e32 v164, v46
	v_cvt_f32_f16_sdwa v165, v46 dst_sel:DWORD dst_unused:UNUSED_PAD src0_sel:WORD_1
	v_fmac_f32_e32 v144, v151, v164
	v_fmac_f32_e32 v145, v151, v165
	v_cvt_f32_f16_e32 v164, v47
	v_cvt_f32_f16_sdwa v165, v47 dst_sel:DWORD dst_unused:UNUSED_PAD src0_sel:WORD_1
	v_fmac_f32_e32 v146, v151, v164
	v_fmac_f32_e32 v147, v151, v165
	v_fmac_f32_e32 v166, v151, v159
	v_cvt_f32_f16_e32 v164, v48
	v_cvt_f32_f16_sdwa v165, v48 dst_sel:DWORD dst_unused:UNUSED_PAD src0_sel:WORD_1
	v_fmac_f32_e32 v140, v152, v164
	v_fmac_f32_e32 v141, v152, v165
	v_cvt_f32_f16_e32 v164, v49
	v_cvt_f32_f16_sdwa v165, v49 dst_sel:DWORD dst_unused:UNUSED_PAD src0_sel:WORD_1
	v_fmac_f32_e32 v142, v152, v164
	v_fmac_f32_e32 v143, v152, v165
	v_cvt_f32_f16_e32 v164, v50
	v_cvt_f32_f16_sdwa v165, v50 dst_sel:DWORD dst_unused:UNUSED_PAD src0_sel:WORD_1
	v_fmac_f32_e32 v144, v152, v164
	v_fmac_f32_e32 v145, v152, v165
	v_cvt_f32_f16_e32 v164, v51
	v_cvt_f32_f16_sdwa v165, v51 dst_sel:DWORD dst_unused:UNUSED_PAD src0_sel:WORD_1
	v_fmac_f32_e32 v146, v152, v164
	v_fmac_f32_e32 v147, v152, v165
	v_fmac_f32_e32 v166, v152, v160
	v_cvt_f32_f16_e32 v164, v52
	v_cvt_f32_f16_sdwa v165, v52 dst_sel:DWORD dst_unused:UNUSED_PAD src0_sel:WORD_1
	v_fmac_f32_e32 v140, v153, v164
	v_fmac_f32_e32 v141, v153, v165
	v_cvt_f32_f16_e32 v164, v53
	v_cvt_f32_f16_sdwa v165, v53 dst_sel:DWORD dst_unused:UNUSED_PAD src0_sel:WORD_1
	v_fmac_f32_e32 v142, v153, v164
	v_fmac_f32_e32 v143, v153, v165
	v_cvt_f32_f16_e32 v164, v54
	v_cvt_f32_f16_sdwa v165, v54 dst_sel:DWORD dst_unused:UNUSED_PAD src0_sel:WORD_1
	v_fmac_f32_e32 v144, v153, v164
	v_fmac_f32_e32 v145, v153, v165
	v_cvt_f32_f16_e32 v164, v55
	v_cvt_f32_f16_sdwa v165, v55 dst_sel:DWORD dst_unused:UNUSED_PAD src0_sel:WORD_1
	v_fmac_f32_e32 v146, v153, v164
	v_fmac_f32_e32 v147, v153, v165
	v_fmac_f32_e32 v166, v153, v161
	v_cvt_f32_f16_e32 v164, v56
	v_cvt_f32_f16_sdwa v165, v56 dst_sel:DWORD dst_unused:UNUSED_PAD src0_sel:WORD_1
	v_fmac_f32_e32 v140, v154, v164
	v_fmac_f32_e32 v141, v154, v165
	v_cvt_f32_f16_e32 v164, v57
	v_cvt_f32_f16_sdwa v165, v57 dst_sel:DWORD dst_unused:UNUSED_PAD src0_sel:WORD_1
	v_fmac_f32_e32 v142, v154, v164
	v_fmac_f32_e32 v143, v154, v165
	v_cvt_f32_f16_e32 v164, v58
	v_cvt_f32_f16_sdwa v165, v58 dst_sel:DWORD dst_unused:UNUSED_PAD src0_sel:WORD_1
	v_fmac_f32_e32 v144, v154, v164
	v_fmac_f32_e32 v145, v154, v165
	v_cvt_f32_f16_e32 v164, v59
	v_cvt_f32_f16_sdwa v165, v59 dst_sel:DWORD dst_unused:UNUSED_PAD src0_sel:WORD_1
	v_fmac_f32_e32 v146, v154, v164
	v_fmac_f32_e32 v147, v154, v165
	v_fmac_f32_e32 v166, v154, v162
	v_cvt_f32_f16_e32 v164, v60
	v_cvt_f32_f16_sdwa v165, v60 dst_sel:DWORD dst_unused:UNUSED_PAD src0_sel:WORD_1
	v_fmac_f32_e32 v140, v155, v164
	v_fmac_f32_e32 v141, v155, v165
	v_cvt_f32_f16_e32 v164, v61
	v_cvt_f32_f16_sdwa v165, v61 dst_sel:DWORD dst_unused:UNUSED_PAD src0_sel:WORD_1
	v_fmac_f32_e32 v142, v155, v164
	v_fmac_f32_e32 v143, v155, v165
	v_cvt_f32_f16_e32 v164, v62
	v_cvt_f32_f16_sdwa v165, v62 dst_sel:DWORD dst_unused:UNUSED_PAD src0_sel:WORD_1
	v_fmac_f32_e32 v144, v155, v164
	v_fmac_f32_e32 v145, v155, v165
	v_cvt_f32_f16_e32 v164, v63
	v_cvt_f32_f16_sdwa v165, v63 dst_sel:DWORD dst_unused:UNUSED_PAD src0_sel:WORD_1
	v_fmac_f32_e32 v146, v155, v164
	v_fmac_f32_e32 v147, v155, v165
	v_fmac_f32_e32 v166, v155, v163
	v_add_f32_dpp v140, v140, v140 row_ror:8 row_mask:0xf bank_mask:0xf
	v_add_f32_dpp v141, v141, v141 row_ror:8 row_mask:0xf bank_mask:0xf
	v_add_f32_dpp v142, v142, v142 row_ror:8 row_mask:0xf bank_mask:0xf
	v_add_f32_dpp v143, v143, v143 row_ror:8 row_mask:0xf bank_mask:0xf
	v_add_f32_dpp v144, v144, v144 row_ror:8 row_mask:0xf bank_mask:0xf
	v_add_f32_dpp v145, v145, v145 row_ror:8 row_mask:0xf bank_mask:0xf
	v_add_f32_dpp v146, v146, v146 row_ror:8 row_mask:0xf bank_mask:0xf
	v_add_f32_dpp v147, v147, v147 row_ror:8 row_mask:0xf bank_mask:0xf
	v_add_f32_dpp v166, v166, v166 row_ror:8 row_mask:0xf bank_mask:0xf
	v_add_f32_dpp v140, v140, v140 row_ror:4 row_mask:0xf bank_mask:0xf
	v_add_f32_dpp v141, v141, v141 row_ror:4 row_mask:0xf bank_mask:0xf
	v_add_f32_dpp v142, v142, v142 row_ror:4 row_mask:0xf bank_mask:0xf
	v_add_f32_dpp v143, v143, v143 row_ror:4 row_mask:0xf bank_mask:0xf
	v_add_f32_dpp v144, v144, v144 row_ror:4 row_mask:0xf bank_mask:0xf
	v_add_f32_dpp v145, v145, v145 row_ror:4 row_mask:0xf bank_mask:0xf
	v_add_f32_dpp v146, v146, v146 row_ror:4 row_mask:0xf bank_mask:0xf
	v_add_f32_dpp v147, v147, v147 row_ror:4 row_mask:0xf bank_mask:0xf
	v_add_f32_dpp v166, v166, v166 row_ror:4 row_mask:0xf bank_mask:0xf
	v_add_f32_dpp v140, v140, v140 row_ror:2 row_mask:0xf bank_mask:0xf
	v_add_f32_dpp v141, v141, v141 row_ror:2 row_mask:0xf bank_mask:0xf
	v_add_f32_dpp v142, v142, v142 row_ror:2 row_mask:0xf bank_mask:0xf
	v_add_f32_dpp v143, v143, v143 row_ror:2 row_mask:0xf bank_mask:0xf
	v_add_f32_dpp v144, v144, v144 row_ror:2 row_mask:0xf bank_mask:0xf
	v_add_f32_dpp v145, v145, v145 row_ror:2 row_mask:0xf bank_mask:0xf
	v_add_f32_dpp v146, v146, v146 row_ror:2 row_mask:0xf bank_mask:0xf
	v_add_f32_dpp v147, v147, v147 row_ror:2 row_mask:0xf bank_mask:0xf
	v_add_f32_dpp v166, v166, v166 row_ror:2 row_mask:0xf bank_mask:0xf
	v_add_f32_dpp v140, v140, v140 row_ror:1 row_mask:0xf bank_mask:0xf
	v_add_f32_dpp v141, v141, v141 row_ror:1 row_mask:0xf bank_mask:0xf
	v_add_f32_dpp v142, v142, v142 row_ror:1 row_mask:0xf bank_mask:0xf
	v_add_f32_dpp v143, v143, v143 row_ror:1 row_mask:0xf bank_mask:0xf
	v_add_f32_dpp v144, v144, v144 row_ror:1 row_mask:0xf bank_mask:0xf
	v_add_f32_dpp v145, v145, v145 row_ror:1 row_mask:0xf bank_mask:0xf
	v_add_f32_dpp v146, v146, v146 row_ror:1 row_mask:0xf bank_mask:0xf
	v_add_f32_dpp v147, v147, v147 row_ror:1 row_mask:0xf bank_mask:0xf
	v_add_f32_dpp v166, v166, v166 row_ror:1 row_mask:0xf bank_mask:0xf
	v_cvt_pk_f16_f32 v252, v140, v141
	v_cvt_pk_f16_f32 v253, v142, v143
	v_cvt_pk_f16_f32 v254, v144, v145
	v_cvt_pk_f16_f32 v255, v146, v147
	s_waitcnt lgkmcnt(0)
	v_add_f32_e32 v209, s12, v166
	v_add_u32_e32 v220, s18, v102
	v_add_u32_e32 v220, s18, v220
	v_min_u32_e32 v218, s19, v220
	v_lshlrev_b32_e32 v218, 9, v218
	v_lshl_add_u64 v[216:217], v[222:223], 0, v[218:219]
	global_load_dword v228, v[216:217], off nt
	global_load_dword v229, v[216:217], off offset:128 nt
	global_load_dword v230, v[216:217], off offset:256 nt
	global_load_dword v231, v[216:217], off offset:384 nt
	v_add_u32_e32 v220, s18, v220
	v_min_u32_e32 v218, s19, v220
	v_lshlrev_b32_e32 v218, 9, v218
	v_lshl_add_u64 v[216:217], v[222:223], 0, v[218:219]
	global_load_dword v232, v[216:217], off nt
	global_load_dword v233, v[216:217], off offset:128 nt
	global_load_dword v234, v[216:217], off offset:256 nt
	global_load_dword v235, v[216:217], off offset:384 nt
	v_add_u32_e32 v220, s18, v220
	v_min_u32_e32 v218, s19, v220
	v_lshlrev_b32_e32 v218, 9, v218
	v_lshl_add_u64 v[216:217], v[222:223], 0, v[218:219]
	global_load_dword v236, v[216:217], off nt
	global_load_dword v237, v[216:217], off offset:128 nt
	global_load_dword v238, v[216:217], off offset:256 nt
	global_load_dword v239, v[216:217], off offset:384 nt
	v_add_u32_e32 v220, s18, v220
	v_min_u32_e32 v218, s19, v220
	v_lshlrev_b32_e32 v218, 9, v218
	v_lshl_add_u64 v[216:217], v[222:223], 0, v[218:219]
	global_load_dword v240, v[216:217], off nt
	global_load_dword v241, v[216:217], off offset:128 nt
	global_load_dword v242, v[216:217], off offset:256 nt
	global_load_dword v243, v[216:217], off offset:384 nt
	v_add_u32_e32 v220, s18, v220
	v_min_u32_e32 v218, s19, v220
	v_lshlrev_b32_e32 v218, 9, v218
	v_lshl_add_u64 v[216:217], v[222:223], 0, v[218:219]
	global_load_dword v244, v[216:217], off nt
	global_load_dword v245, v[216:217], off offset:128 nt
	global_load_dword v246, v[216:217], off offset:256 nt
	global_load_dword v247, v[216:217], off offset:384 nt
	v_add_u32_e32 v220, s18, v220
	v_min_u32_e32 v218, s19, v220
	v_lshlrev_b32_e32 v218, 9, v218
	v_lshl_add_u64 v[216:217], v[222:223], 0, v[218:219]
	global_load_dword v248, v[216:217], off nt
	global_load_dword v249, v[216:217], off offset:128 nt
	global_load_dword v250, v[216:217], off offset:256 nt
	global_load_dword v251, v[216:217], off offset:384 nt
	s_waitcnt vmcnt(24)

	.amdhsa_kernel _Z5k_decPKiPKDF16_S2_PKfS4_S4_Pf
		.amdhsa_group_segment_fixed_size 45056
		.amdhsa_private_segment_fixed_size 0
		.amdhsa_kernarg_size 312
		.amdhsa_user_sgpr_count 2
		.amdhsa_user_sgpr_dispatch_ptr 0
		.amdhsa_user_sgpr_queue_ptr 0
		.amdhsa_user_sgpr_kernarg_segment_ptr 1
		.amdhsa_user_sgpr_dispatch_id 0
		.amdhsa_user_sgpr_kernarg_preload_length 0
		.amdhsa_user_sgpr_kernarg_preload_offset 0
		.amdhsa_user_sgpr_private_segment_size 0
		.amdhsa_uses_dynamic_stack 0
		.amdhsa_enable_private_segment 0
		.amdhsa_system_sgpr_workgroup_id_x 1
		.amdhsa_system_sgpr_workgroup_id_y 0
		.amdhsa_system_sgpr_workgroup_id_z 0
		.amdhsa_system_sgpr_workgroup_info 0
		.amdhsa_system_vgpr_workitem_id 0
		.amdhsa_next_free_vgpr 256
		.amdhsa_next_free_sgpr 96
		.amdhsa_accum_offset 256
		.amdhsa_reserve_vcc 1
		.amdhsa_float_round_mode_32 0
		.amdhsa_float_round_mode_16_64 0
		.amdhsa_float_denorm_mode_32 3
		.amdhsa_float_denorm_mode_16_64 3
		.amdhsa_dx10_clamp 1
		.amdhsa_ieee_mode 1
		.amdhsa_fp16_overflow 0
		.amdhsa_tg_split 0
		.amdhsa_exception_fp_ieee_invalid_op 0
		.amdhsa_exception_fp_denorm_src 0
		.amdhsa_exception_fp_ieee_div_zero 0
		.amdhsa_exception_fp_ieee_overflow 0
		.amdhsa_exception_fp_ieee_underflow 0
		.amdhsa_exception_fp_ieee_inexact 0
		.amdhsa_exception_int_div_zero 0
	.end_amdhsa_kernel

amdhsa.kernels:
  - .agpr_count:     0
    .args:
      - .actual_access:  read_only
        .address_space:  global
        .offset:         0
        .size:           8
        .value_kind:     global_buffer
      - .actual_access:  read_only
        .address_space:  global
        .offset:         8
        .size:           8
        .value_kind:     global_buffer
      - .actual_access:  write_only
        .address_space:  global
        .offset:         16
        .size:           8
        .value_kind:     global_buffer
      - .actual_access:  read_only
        .address_space:  global
        .offset:         24
        .size:           8
        .value_kind:     global_buffer
      - .actual_access:  write_only
        .address_space:  global
        .offset:         32
        .size:           8
        .value_kind:     global_buffer
      - .actual_access:  write_only
        .address_space:  global
        .offset:         40
        .size:           8
        .value_kind:     global_buffer
      - .actual_access:  read_only
        .address_space:  global
        .offset:         48
        .size:           8
        .value_kind:     global_buffer
      - .actual_access:  read_only
        .address_space:  global
        .offset:         56
        .size:           8
        .value_kind:     global_buffer
      - .actual_access:  write_only
        .address_space:  global
        .offset:         64
        .size:           8
        .value_kind:     global_buffer
    .group_segment_fixed_size: 53904
    .kernarg_segment_align: 8
    .kernarg_segment_size: 72
    .language:       OpenCL C
    .language_version:
      - 2
      - 0
    .max_flat_workgroup_size: 1024
    .name:           _Z6k_partPKiS0_PiS1_PjS1_PKfS4_Pf
    .private_segment_fixed_size: 0
    .sgpr_count:     31
    .sgpr_spill_count: 0
    .symbol:         _Z6k_partPKiS0_PiS1_PjS1_PKfS4_Pf.kd
    .uniform_work_group_size: 1
    .uses_dynamic_stack: false
    .vgpr_count:     64
    .vgpr_spill_count: 0
    .wavefront_size: 64
  - .agpr_count:     0
    .args:
      - .actual_access:  read_only
        .address_space:  global
        .offset:         0
        .size:           8
        .value_kind:     global_buffer
      - .actual_access:  read_only
        .address_space:  global
        .offset:         8
        .size:           8
        .value_kind:     global_buffer
      - .actual_access:  read_only
        .address_space:  global
        .offset:         16
        .size:           8
        .value_kind:     global_buffer
      - .address_space:  global
        .offset:         24
        .size:           8
        .value_kind:     global_buffer
      - .actual_access:  read_only
        .address_space:  global
        .offset:         32
        .size:           8
        .value_kind:     global_buffer
      - .actual_access:  write_only
        .address_space:  global
        .offset:         40
        .size:           8
        .value_kind:     global_buffer
      - .actual_access:  write_only
        .address_space:  global
        .offset:         48
        .size:           8
        .value_kind:     global_buffer
      - .actual_access:  write_only
        .address_space:  global
        .offset:         56
        .size:           8
        .value_kind:     global_buffer
      - .actual_access:  write_only
        .address_space:  global
        .offset:         64
        .size:           8
        .value_kind:     global_buffer
      - .actual_access:  write_only
        .address_space:  global
        .offset:         72
        .size:           8
        .value_kind:     global_buffer
      - .actual_access:  read_only
        .address_space:  global
        .offset:         80
        .size:           8
        .value_kind:     global_buffer
      - .actual_access:  read_only
        .address_space:  global
        .offset:         88
        .size:           8
        .value_kind:     global_buffer
      - .actual_access:  read_only
        .address_space:  global
        .offset:         96
        .size:           8
        .value_kind:     global_buffer
      - .actual_access:  read_only
        .address_space:  global
        .offset:         104
        .size:           8
        .value_kind:     global_buffer
      - .actual_access:  write_only
        .address_space:  global
        .offset:         112
        .size:           8
        .value_kind:     global_buffer
      - .actual_access:  write_only
        .address_space:  global
        .offset:         120
        .size:           8
        .value_kind:     global_buffer
    .group_segment_fixed_size: 38940
    .kernarg_segment_align: 8
    .kernarg_segment_size: 128
    .language:       OpenCL C
    .language_version:
      - 2
      - 0
    .max_flat_workgroup_size: 1024
    .name:           _Z5k_csrPKjPKiS2_PiPKfPfPDF16_S3_S3_S3_S5_S5_S5_S5_S7_S6_
    .private_segment_fixed_size: 0
    .sgpr_count:     72
    .sgpr_spill_count: 0
    .symbol:         _Z5k_csrPKjPKiS2_PiPKfPfPDF16_S3_S3_S3_S5_S5_S5_S5_S7_S6_.kd
    .uniform_work_group_size: 1
    .uses_dynamic_stack: false
    .vgpr_count:     64
    .vgpr_spill_count: 0
    .wavefront_size: 64
  - .agpr_count:     0
    .args:
      - .actual_access:  read_only
        .address_space:  global
        .offset:         0
        .size:           8
        .value_kind:     global_buffer
      - .actual_access:  read_only
        .address_space:  global
        .offset:         8
        .size:           8
        .value_kind:     global_buffer
      - .actual_access:  read_only
        .address_space:  global
        .offset:         16
        .size:           8
        .value_kind:     global_buffer
      - .actual_access:  read_only
        .address_space:  global
        .offset:         24
        .size:           8
        .value_kind:     global_buffer
      - .actual_access:  read_only
        .address_space:  global
        .offset:         32
        .size:           8
        .value_kind:     global_buffer
      - .actual_access:  read_only
        .address_space:  global
        .offset:         40
        .size:           8
        .value_kind:     global_buffer
      - .actual_access:  write_only
        .address_space:  global
        .offset:         48
        .size:           8
        .value_kind:     global_buffer
      - .offset:         56
        .size:           4
        .value_kind:     hidden_block_count_x
      - .offset:         60
        .size:           4
        .value_kind:     hidden_block_count_y
      - .offset:         64
        .size:           4
        .value_kind:     hidden_block_count_z
      - .offset:         68
        .size:           2
        .value_kind:     hidden_group_size_x
      - .offset:         70
        .size:           2
        .value_kind:     hidden_group_size_y
      - .offset:         72
        .size:           2
        .value_kind:     hidden_group_size_z
      - .offset:         74
        .size:           2
        .value_kind:     hidden_remainder_x
      - .offset:         76
        .size:           2
        .value_kind:     hidden_remainder_y
      - .offset:         78
        .size:           2
        .value_kind:     hidden_remainder_z
      - .offset:         96
        .size:           8
        .value_kind:     hidden_global_offset_x
      - .offset:         104
        .size:           8
        .value_kind:     hidden_global_offset_y
      - .offset:         112
        .size:           8
        .value_kind:     hidden_global_offset_z
      - .offset:         120
        .size:           2
        .value_kind:     hidden_grid_dims
    .group_segment_fixed_size: 45056
    .kernarg_segment_align: 8
    .kernarg_segment_size: 312
    .language:       OpenCL C
    .language_version:
      - 2
      - 0
    .max_flat_workgroup_size: 256
    .name:           _Z5k_decPKiPKDF16_S2_PKfS4_S4_Pf
    .private_segment_fixed_size: 0
    .sgpr_count:     28
    .sgpr_spill_count: 0
    .symbol:         _Z5k_decPKiPKDF16_S2_PKfS4_S4_Pf.kd
    .uniform_work_group_size: 1
    .uses_dynamic_stack: false
    .vgpr_count:     256
    .vgpr_spill_count: 0
    .wavefront_size: 64
  - .agpr_count:     0
    .args:
      - .actual_access:  read_only
        .address_space:  global
        .offset:         0
        .size:           8
        .value_kind:     global_buffer
      - .actual_access:  read_only
        .address_space:  global
        .offset:         8
        .size:           8
        .value_kind:     global_buffer
      - .actual_access:  read_only
        .address_space:  global
        .offset:         16
        .size:           8
        .value_kind:     global_buffer
      - .actual_access:  read_only
        .address_space:  global
        .offset:         24
        .size:           8
        .value_kind:     global_buffer
      - .actual_access:  read_only
        .address_space:  global
        .offset:         32
        .size:           8
        .value_kind:     global_buffer
      - .actual_access:  read_only
        .address_space:  global
        .offset:         40
        .size:           8
        .value_kind:     global_buffer
      - .actual_access:  write_only
        .address_space:  global
        .offset:         48
        .size:           8
        .value_kind:     global_buffer
      - .actual_access:  read_only
        .address_space:  global
        .offset:         56
        .size:           8
        .value_kind:     global_buffer
    .group_segment_fixed_size: 0
    .kernarg_segment_align: 8
    .kernarg_segment_size: 64
    .language:       OpenCL C
    .language_version:
      - 2
      - 0
    .max_flat_workgroup_size: 64
    .name:           _Z5k_aggILi1EEvPKiS1_S1_PKDv4_jPKfS6_PS2_PDF16_
    .private_segment_fixed_size: 0
    .sgpr_count:     82
    .sgpr_spill_count: 0
    .symbol:         _Z5k_aggILi1EEvPKiS1_S1_PKDv4_jPKfS6_PS2_PDF16_.kd
    .uniform_work_group_size: 1
    .uses_dynamic_stack: false
    .vgpr_count:     72
    .vgpr_spill_count: 0
    .wavefront_size: 64
  - .agpr_count:     0
    .args:
      - .actual_access:  read_only
        .address_space:  global
        .offset:         0
        .size:           8
        .value_kind:     global_buffer
      - .actual_access:  read_only
        .address_space:  global
        .offset:         8
        .size:           8
        .value_kind:     global_buffer
      - .actual_access:  read_only
        .address_space:  global
        .offset:         16
        .size:           8
        .value_kind:     global_buffer
      - .actual_access:  read_only
        .address_space:  global
        .offset:         24
        .size:           8
        .value_kind:     global_buffer
      - .actual_access:  read_only
        .address_space:  global
        .offset:         32
        .size:           8
        .value_kind:     global_buffer
      - .actual_access:  read_only
        .address_space:  global
        .offset:         40
        .size:           8
        .value_kind:     global_buffer
      - .actual_access:  read_only
        .address_space:  global
        .offset:         48
        .size:           8
        .value_kind:     global_buffer
      - .actual_access:  write_only
        .address_space:  global
        .offset:         56
        .size:           8
        .value_kind:     global_buffer
    .group_segment_fixed_size: 0
    .kernarg_segment_align: 8
    .kernarg_segment_size: 64
    .language:       OpenCL C
    .language_version:
      - 2
      - 0
    .max_flat_workgroup_size: 64
    .name:           _Z5k_aggILi2EEvPKiS1_S1_PKDv4_jPKfS6_PS2_PDF16_
    .private_segment_fixed_size: 0
    .sgpr_count:     66
    .sgpr_spill_count: 0
    .symbol:         _Z5k_aggILi2EEvPKiS1_S1_PKDv4_jPKfS6_PS2_PDF16_.kd
    .uniform_work_group_size: 1
    .uses_dynamic_stack: false
    .vgpr_count:     72
    .vgpr_spill_count: 0
    .wavefront_size: 64
